# v33 + prep_moe deal: heavy workgroups (extra in-proj unit) convert nothing ahead of their GEMM; light ones take 6 item slots (1 ahead, 5 behind)
# speedup vs baseline: 1.0096x; 1.0096x over previous
; template <class Tp> __device__ __forceinline__ Tp* wsp(const Frame& F, size_t off) { return (Tp*)(F.ws + off); }
; __device__ __forceinline__ void phase_prep_moe(Frame& F, int l, int part) {
;     ...
;     constexpr int I_G1 = 16 * 8, I_DN = 4 * 16, I_E = I_G1 + I_DN;
;     bf16_t* WG1 = wsp<bf16_t>(F, WS_WG1); bf16_t* WD = wsp<bf16_t>(F, WS_WD);
;     const int nextra = ((T / 256) * (INP / 256)) % F.G, nlight = F.G - nextra;
;     const int slots = (nextra ? nextra : 0) * NWAVES + nlight * NWAVES * (nextra ? 5 : 1);
;     const bool light = F.bx >= nextra; const int mult = (light && nextra) ? 5 : 1;
;     const int base = light ? nextra * NWAVES + ((F.bx - nextra) * NWAVES + F.wave) * mult : F.bx * NWAVES + F.wave;
;     const int k0 = part ? 1 : 0, k1 = part ? mult : 1;
.LBB0_283:
	s_or_b64 exec, exec, s[24:25]
	s_abs_i32 s3, s76
	v_cvt_f32_u32_e32 v1, s3
	s_sub_i32 s4, 0, s3
	s_load_dwordx2 s[16:17], s[0:1], 0x60
	s_load_dwordx4 s[24:27], s[0:1], 0x0
	v_readlane_b32 s22, v253, 2
	v_rcp_iflag_f32_e32 v1, v1
	s_movk_i32 s14, 0x91
	s_mov_b32 s89, 0
	s_mov_b32 s73, s89
	v_mul_f32_e32 v1, 0x4f7ffffe, v1
	v_cvt_u32_f32_e32 v1, v1
	v_mov_b32_e32 v188, v0
	v_and_b32_e32 v2, 32, v0
	v_and_b32_e32 v0, 16, v0
	v_readfirstlane_b32 s5, v1
	s_mul_i32 s4, s4, s5
	s_mul_hi_u32 s4, s5, s4
	s_add_i32 s5, s5, s4
	s_mul_hi_u32 s4, s5, 0x480
	s_mul_i32 s4, s4, s3
	s_sub_i32 s4, 0x480, s4
	s_sub_i32 s6, s4, s3
	s_cmp_ge_u32 s4, s3
	s_cselect_b32 s4, s6, s4
	s_sub_i32 s6, s4, s3
	s_cmp_ge_u32 s4, s3
	s_cselect_b32 s7, s6, s4
	s_lshl_b32 s6, s7, 3
	s_cmp_lg_u32 s7, 0
	s_cselect_b64 s[10:11], -1, 0
	s_and_b64 s[8:9], s[10:11], exec
	s_cselect_b32 s8, 6, 1
	s_cmp_ge_i32 s77, s7
	s_cselect_b64 s[12:13], -1, 0
	s_and_b64 s[10:11], s[10:11], s[12:13]
	s_and_b64 s[10:11], s[10:11], exec
	s_cselect_b32 s70, 6, 1
	s_cmp_lt_i32 s77, s7
	s_cselect_b32 s70, 0, s70
	s_sub_i32 s4, s77, s7
	s_lshl_b32 s4, s4, 3
	s_add_i32 s4, s4, s72
	s_mul_i32 s4, s4, s70
	s_cmp_ge_i32 s77, s7
	s_cselect_b64 s[10:11], -1, 0
	s_and_b64 s[10:11], s[10:11], exec
	s_cselect_b32 s71, s4, s22
	s_waitcnt lgkmcnt(0)
	s_cmp_lg_u64 s[16:17], 0
	s_cselect_b64 s[92:93], -1, 0
	s_cmpk_lt_i32 s77, 0x480
	s_cselect_b64 s[10:11], -1, 0
	s_ashr_i32 s23, s77, 31
	s_lshr_b32 s4, s23, 29
	s_add_i32 s4, s77, s4
	s_ashr_i32 s16, s4, 3
	s_and_b32 s4, s4, -8
	s_sub_i32 s17, s77, s4
	s_lshl_b32 s4, s17, 6
	s_cmp_lt_i32 s17, 0
	v_writelane_b32 v253, s10, 6
	s_cselect_b32 s9, s14, 0x90
	s_mul_i32 s9, s9, s17
	v_writelane_b32 v253, s11, 7
	s_mul_i32 s10, s17, 0x41
	s_cselect_b32 s18, 49, 48
	s_cselect_b32 s19, s10, s4
	s_add_i32 s9, s9, s16
	s_mul_hi_i32 s4, s9, 0x38e38e39
	s_lshr_b32 s10, s4, 31
	s_ashr_i32 s4, s4, 4
	s_add_i32 s4, s4, s10
	s_mul_i32 s10, s4, 0x48
	s_sub_i32 s9, s9, s10
	s_lshl_b32 s11, s4, 3
	s_bfe_i32 s4, s9, 0x80000
	s_bfe_u32 s4, s4, 0x3000c
	s_add_i32 s10, s9, s4
	s_bfe_i32 s4, s10, 0x80000
	s_and_b32 s10, s10, 0xf8
	s_sub_i32 s9, s9, s10
	s_sext_i32_i16 s12, s4
	s_sext_i32_i8 s9, s9
	s_add_i32 s24, s11, s9
	s_ashr_i32 s9, s12, 3
	s_lshr_b32 s4, s12, 3
	v_writelane_b32 v253, s9, 8
	s_ashr_i32 s25, s76, 31
	s_and_b32 s9, s76, 15
	s_ashr_i32 s14, s76, 1
	s_cmp_lg_u32 s9, 0
	s_cselect_b64 s[10:11], -1, 0
	s_and_b64 s[12:13], s[10:11], exec
	s_cselect_b32 s28, s76, s14
	s_cselect_b32 s9, 0, s14
	s_cmp_ge_i32 s77, s28
	s_cselect_b64 s[12:13], -1, 0
	s_cmp_lt_i32 s77, s28
	s_cselect_b64 s[14:15], -1, 0
	s_or_b64 s[14:15], s[10:11], s[14:15]
	v_writelane_b32 v253, s14, 9
	s_cmpk_lt_i32 s77, 0x180
	s_nop 0
	v_writelane_b32 v253, s15, 10
	s_cselect_b64 s[14:15], -1, 0
	v_writelane_b32 v253, s14, 11
	s_or_b64 s[10:11], s[10:11], s[12:13]
	s_ashr_i32 s30, s28, 31
	v_writelane_b32 v253, s15, 12
	s_mul_i32 s14, s18, s17
	s_add_i32 s14, s14, s16
	s_mul_hi_i32 s15, s14, 0x2aaaaaab
	s_lshr_b32 s18, s15, 31
	s_ashr_i32 s15, s15, 2
	s_add_i32 s15, s15, s18
	s_mul_i32 s18, s15, 24
	s_sub_i32 s14, s14, s18
	s_bfe_i32 s18, s14, 0x80000
	s_bfe_u32 s18, s18, 0x3000c
	s_add_i32 s18, s14, s18
	s_bfe_i32 s20, s18, 0x80000
	s_and_b32 s18, s18, 0xf8
	s_sub_i32 s14, s14, s18
	s_lshl_b32 s15, s15, 3
	s_sext_i32_i16 s20, s20
	s_sext_i32_i8 s14, s14
	s_add_i32 s29, s15, s14
	s_ashr_i32 s14, s20, 3
	v_writelane_b32 v253, s14, 13
	v_writelane_b32 v253, s10, 14
	s_barrier
	s_nop 0
	v_writelane_b32 v253, s11, 15
	s_sub_i32 s10, s77, s9
	s_cmpk_lt_i32 s10, 0x200
	s_cselect_b64 s[12:13], -1, 0
	s_ashr_i32 s11, s10, 31
	s_lshr_b32 s11, s11, 29
	s_add_i32 s11, s10, s11
	s_ashr_i32 s18, s11, 3
	s_and_b32 s11, s11, -8
	v_writelane_b32 v253, s12, 16
	s_sub_i32 s20, s10, s11
	s_lshl_b32 s21, s20, 6
	v_writelane_b32 v253, s13, 17
	s_and_b32 s12, s76, 7
	s_cmp_lg_u32 s12, 0
	s_cselect_b64 s[90:91], -1, 0
	s_ashr_i32 s10, s76, 3
	v_writelane_b32 v253, s10, 18
	s_mul_i32 s10, s10, s17
	s_add_i32 s17, s10, s16
	s_cmpk_lt_i32 s77, 0x200
	s_mul_i32 s11, s72, 0xc40
	s_cselect_b64 s[14:15], -1, 0
	v_writelane_b32 v253, s14, 19
	s_add_i32 s10, s11, 0
	s_add_i32 s10, s10, 0x12400
	v_writelane_b32 v253, s15, 20
	v_writelane_b32 v253, s10, 21
	s_lshl_b32 s10, s76, 3
	s_cmpk_lt_u32 s2, 0x1240
	s_cselect_b64 s[94:95], -1, 0
	s_cmp_lt_i32 s22, 0x8000
	v_writelane_b32 v253, s10, 22
	s_cselect_b64 s[10:11], -1, 0
	v_writelane_b32 v253, s10, 23
	s_lshl_b32 s2, s76, 7
	s_ashr_i32 s31, s77, 3
	v_writelane_b32 v253, s11, 24
	v_writelane_b32 v253, s2, 25
	s_lshl_b32 s2, s72, 9
	s_add_i32 s2, s2, 0
	s_add_i32 s2, s2, 0x18700
	v_writelane_b32 v253, s2, 26
	s_lshr_b32 s2, s77, 31
	s_add_i32 s10, s77, s2
	s_ashr_i32 s11, s10, 1
	s_and_b32 s10, s10, -2
	v_writelane_b32 v253, s11, 27
	s_sub_i32 s10, s77, s10
	s_add_i32 s2, s31, s2
	v_writelane_b32 v253, s10, 28
	s_ashr_i32 s10, s2, 1
	s_and_b32 s2, s2, -2
	s_lshl_b32 s22, s76, 4
	s_and_b32 s65, s77, 7
	s_sub_i32 s2, s31, s2
	s_cmpk_gt_i32 s76, 0x7f
	v_writelane_b32 v253, s10, 29
	s_cselect_b64 s[10:11], -1, 0
	s_cmp_eq_u32 s12, 0
	s_cselect_b64 s[12:13], -1, 0
	s_and_b64 s[14:15], s[12:13], exec
	v_writelane_b32 v253, s2, 30
	s_cselect_b32 s79, s17, s77
	s_and_b64 s[10:11], s[10:11], s[12:13]
	v_writelane_b32 v253, s10, 31
	s_cmp_gt_i32 s77, 63
	v_mov_b32_e32 v1, 0
	v_writelane_b32 v253, s11, 32
	s_cselect_b64 s[10:11], -1, 0
	s_and_b32 s12, s77, 0x7ffffff8
	s_sub_i32 s17, s76, 64
	s_sub_i32 s13, s12, 64
	v_writelane_b32 v253, s10, 33
	s_cmpk_lt_u32 s13, 0x200
	v_mov_b32_e32 v236, 0x358637bd
	v_writelane_b32 v253, s11, 34
	s_cselect_b64 s[10:11], -1, 0
	v_writelane_b32 v253, s10, 35
; __device__ __forceinline__ void phase_prep_moe(Frame& F, int l, int part) {
;     ...
;     const int nextra = ((T / 256) * (INP / 256)) % F.G, nlight = F.G - nextra;
;     const int slots = (nextra ? nextra : 0) * NWAVES + nlight * NWAVES * (nextra ? 5 : 1);
;     const bool light = F.bx >= nextra; const int mult = (light && nextra) ? 5 : 1;
;     const int base = light ? nextra * NWAVES + ((F.bx - nextra) * NWAVES + F.wave) * mult : F.bx * NWAVES + F.wave;
;     const int k0 = part ? 1 : 0, k1 = part ? mult : 1;
	s_lshr_b32 s2, s13, 3
	s_bfe_u32 s14, s13, 0x20006
	v_writelane_b32 v253, s11, 36
	s_lshl_b32 s10, s77, 6
	s_add_i32 s2, s2, s10
	s_lshr_b32 s2, s2, 2
	s_and_b32 s2, s2, 0x78
	s_bfe_u32 s10, s13, 0x30003
	s_or_b32 s2, s2, s10
	v_writelane_b32 v253, s2, 37
	s_lshl_b32 s2, s2, 8
	v_writelane_b32 v253, s2, 38
	s_bitset1_b32 s2, 7
	v_writelane_b32 v253, s2, 39
	s_lshr_b32 s2, s23, 30
	s_add_i32 s2, s77, s2
	s_ashr_i32 s10, s2, 2
	s_and_b32 s2, s2, -4
	v_writelane_b32 v253, s10, 40
	s_sub_i32 s2, s77, s2
	v_writelane_b32 v253, s2, 41
	s_lshr_b32 s2, s31, 30
	s_add_i32 s2, s31, s2
	s_ashr_i32 s10, s2, 2
	v_writelane_b32 v253, s10, 42
	s_and_b32 s2, s2, -4
	v_writelane_b32 v253, s31, 43
	s_sub_i32 s2, s31, s2
	s_bfe_i64 s[10:11], s[4:5], 0x100000
	v_writelane_b32 v253, s2, 44
	s_lshl_b64 s[10:11], s[10:11], 19
	v_writelane_b32 v253, s10, 45
	s_lshl_b32 s2, s14, 17
	s_lshl_b32 s34, s76, 9
	v_writelane_b32 v253, s11, 46
	v_writelane_b32 v253, s14, 47
	v_writelane_b32 v253, s2, 48
	v_writelane_b32 v253, s24, 49
	s_lshl_b32 s2, s24, 8
	v_writelane_b32 v253, s2, 50
	s_bitset1_b32 s2, 7
	v_writelane_b32 v253, s2, 51
	v_writelane_b32 v253, s29, 52
	s_lshl_b32 s2, s29, 8
	v_writelane_b32 v253, s2, 53
	s_bitset1_b32 s2, 7
	s_cmp_lt_i32 s20, 0
	s_mulk_i32 s20, 0x41
	v_writelane_b32 v253, s2, 54
	s_cselect_b32 s2, s20, s21
	s_add_i32 s2, s2, s18
	s_ashr_i32 s4, s2, 31
	s_lshr_b32 s4, s4, 27
	s_add_i32 s4, s2, s4
	s_and_b32 s10, s4, 0xffe0
	s_sub_i32 s2, s2, s10
	s_bfe_i32 s10, s2, 0x80000
	s_bfe_u32 s10, s10, 0x3000c
	s_add_i32 s10, s2, s10
	s_and_b32 s11, s10, 0xf8
	s_sub_i32 s2, s2, s11
	s_ashr_i32 s4, s4, 5
	s_lshl_b32 s4, s4, 3
	s_sext_i32_i8 s2, s2
	s_add_i32 s4, s4, s2
	s_bfe_i32 s2, s10, 0x80000
	s_sext_i32_i16 s2, s2
	s_ashr_i32 s10, s2, 3
	s_lshr_b32 s2, s2, 3
	v_writelane_b32 v253, s10, 55
	s_bfe_i64 s[10:11], s[2:3], 0x100000
	s_lshl_b64 s[10:11], s[10:11], 17
	v_writelane_b32 v253, s10, 56
	s_lshl_b32 s2, s4, 8
	v_mov_b32_e32 v251, 0x260
	v_writelane_b32 v253, s11, 57
	v_writelane_b32 v253, s4, 58
	v_writelane_b32 v253, s2, 59
	s_bitset1_b32 s2, 7
	s_cmpk_lt_i32 s79, 0x200
	v_writelane_b32 v253, s2, 60
	s_cselect_b64 s[10:11], -1, 0
	v_writelane_b32 v253, s10, 61
	s_sub_i32 s2, s76, s79
	s_add_i32 s14, s2, 0x1ff
	v_writelane_b32 v253, s11, 62
	s_ashr_i32 s10, s79, 6
	s_lshl_b32 s2, s79, 8
	s_ashr_i32 s11, s10, 31
	s_and_b32 s2, s2, 0x700
	s_lshl_b64 s[20:21], s[10:11], 12
	s_xor_b32 s2, s2, 0xf00
	s_or_b32 s2, s20, s2
	s_bfe_u32 s10, s79, 0x30003
	v_writelane_b32 v253, s2, 63
	s_lshl_b32 s2, s10, 6
	s_cmpk_lt_i32 s79, 0x400
	v_writelane_b32 v254, s2, 0
	s_cselect_b64 s[36:37], -1, 0
	s_add_i32 s2, s19, s16
	s_ashr_i32 s4, s2, 31
	s_lshr_b32 s4, s4, 27
	s_add_i32 s4, s2, s4
	s_and_b32 s11, s4, 0xffe0
	s_sub_i32 s2, s2, s11
	s_bfe_i32 s11, s2, 0x80000
	s_bfe_u32 s11, s11, 0x3000c
	s_add_i32 s11, s2, s11
	s_and_b32 s15, s11, 0xf8
	s_sub_i32 s2, s2, s15
	s_ashr_i32 s4, s4, 5
	s_lshl_b32 s4, s4, 3
	s_sext_i32_i8 s2, s2
	s_add_i32 s15, s4, s2
	s_sub_i32 s2, s76, s7
	s_mul_i32 s2, s2, s8
	s_lshl_b32 s2, s2, 3
	s_mov_b32 s61, s2
	s_abs_i32 s2, s14
	s_mul_hi_u32 s6, s2, s5
	s_mul_i32 s4, s6, s3
	s_sub_i32 s7, s2, s4
	s_bfe_i32 s2, s11, 0x80000
	v_writelane_b32 v254, s36, 1
	s_sext_i32_i16 s2, s2
	s_ashr_i32 s4, s2, 3
	v_writelane_b32 v254, s37, 2
	s_lshr_b32 s2, s2, 3
	v_writelane_b32 v254, s4, 3
	s_bfe_i64 s[4:5], s[2:3], 0x100000
	s_lshl_b64 s[18:19], s[4:5], 17
	v_writelane_b32 v254, s18, 4
	s_lshl_b64 s[4:5], s[4:5], 19
	s_xor_b32 s2, s14, s76
	v_writelane_b32 v254, s19, 5
	v_writelane_b32 v254, s4, 6
	s_ashr_i32 s2, s2, 31
	v_mov_b32_e32 v235, 1
	v_writelane_b32 v254, s5, 7
	v_writelane_b32 v254, s15, 8
	s_lshl_b32 s4, s15, 8
	v_writelane_b32 v254, s4, 9
	s_bitset1_b32 s4, 7
	v_writelane_b32 v254, s4, 10
	s_add_i32 s4, s6, 1
	s_sub_i32 s5, s7, s3
	s_cmp_ge_u32 s7, s3
	s_cselect_b32 s4, s4, s6
	s_cselect_b32 s5, s5, s7
	s_add_i32 s6, s4, 1
	s_cmp_ge_u32 s5, s3
	s_cselect_b32 s3, s6, s4
	s_xor_b32 s3, s3, s2
	s_sub_i32 s2, s3, s2
	s_lshl_b32 s2, s2, 1
	v_writelane_b32 v254, s2, 11
	v_writelane_b32 v254, s28, 12
	s_add_u32 s4, s28, s77
	v_writelane_b32 v254, s30, 13
	s_addc_u32 s5, s30, s23
	s_ashr_i32 s2, s9, 31
	s_sub_u32 s6, s4, s9
	v_writelane_b32 v254, s4, 14
	s_subb_u32 s7, s5, s2
; #define LAS __attribute__((address_space(3)))
; template <class Tp> __device__ __forceinline__ Tp* wsp(const Frame& F, size_t off) { return (Tp*)(F.ws + off); }
; __device__ __forceinline__ void moe_table(Frame& F, int l) {
;     LAS int* tb = (LAS int*)(F.lds + pg8::STAGE_BYTES);
;     __syncthreads();
;     if (F.tid < NEXP) { const unsigned* cnt = wsp<unsigned>(F, WS_CTL) + CW_CNT + 64 * 32 * l;
;         const int c = (int)__hip_atomic_load(cnt + 64 * F.tid, __ATOMIC_RELAXED, __HIP_MEMORY_SCOPE_AGENT); tb[40 + F.tid] = c; tb[80 + F.tid] = (c + 255) >> 8; }
;     __syncthreads();
;     if (F.tid <= NEXP) { int acc = 0; for (int e = 0; e < F.tid; ++e) acc += tb[80 + e]; tb[F.tid] = acc; }
;     __syncthreads();
; }
; __device__ __forceinline__ void phase_moe1(Frame& F, int l) {
;     moe_table(F, l);
;     MoeSched S; S.G = F.G; S.c = F.bx; S.npn = 2; S.gather = 1; S.tb = (const LAS int*)(F.lds + pg8::STAGE_BYTES); S.liste = wsp<int>(F, WS_LISTE); S.Bt = (const char*)(F.ws + WS_WG1); S.K = DM; S.nB = 512;
;     const EpiG1 E{wsp<float>(F, WS_RS), wsp<int>(F, WS_LISTE), wsp<bf16_t>(F, WS_HID)};
;     pg8::gemm_phase(F.lds, F.tid, (const char*)(F.ws + WS_HB), DM, S, E);
; }
; __device__ __forceinline__ void phase_moe2(Frame& F, int l) {
;     MoeSched S; S.G = F.G; S.c = F.bx; S.npn = 4; S.gather = 0; S.tb = (const LAS int*)(F.lds + pg8::STAGE_BYTES); S.liste = wsp<int>(F, WS_LISTE); S.Bt = (const char*)(F.ws + WS_WD); S.K = DEXP; S.nB = 1024;
;     const EpiDn E{wsp<int>(F, WS_LISTE), wsp<float>(F, WS_LISTW), wsp<bf16_t>(F, WS_Y)};
;     pg8::gemm_phase(F.lds, F.tid, (const char*)(F.ws + WS_HID), DEXP, S, E);
; }
	s_lshl_b64 s[2:3], s[72:73], 10
	v_writelane_b32 v254, s5, 15
	v_writelane_b32 v254, s6, 16
	s_add_u32 s4, s2, 0x1000000
	v_mov_b64_e32 v[248:249], 0x480
	v_writelane_b32 v254, s7, 17
	v_writelane_b32 v254, s4, 18
	s_addc_u32 s4, s3, 0
	v_writelane_b32 v254, s4, 19
	s_lshl_b32 s4, s72, 10
	s_add_i32 s58, s4, 0
	s_mov_b32 s4, s72
	v_writelane_b32 v254, s4, 20
	s_add_i32 s55, s72, -8
	s_add_u32 s2, s2, 0x1012400
	v_writelane_b32 v254, s5, 21
	v_writelane_b32 v254, s2, 22
	s_addc_u32 s2, s3, 0
	s_lshl_b32 s3, s65, 2
	s_add_i32 s3, s3, 0
	v_writelane_b32 v254, s2, 23
	s_add_i32 s3, s3, 0x20000
	v_writelane_b32 v254, s3, 24
	s_add_i32 s3, s76, s12
	s_add_i32 s3, s3, s65
	s_add_i32 s4, s3, 0xffffff80
	s_lshl_b32 s3, s76, 6
	s_addk_i32 s3, 0xf000
	v_writelane_b32 v254, s3, 25
	v_writelane_b32 v254, s4, 26
	s_lshl_b32 s4, s4, 6
	s_or_b32 s3, s13, s65
	v_writelane_b32 v254, s4, 27
	v_writelane_b32 v254, s17, 28
	s_add_u32 s3, s3, s17
	v_writelane_b32 v254, s3, 29
	s_addc_u32 s3, 0, 0
	v_writelane_b32 v254, s3, 30
	s_add_u32 s4, s77, s76
	v_writelane_b32 v254, s23, 31
	v_writelane_b32 v254, s25, 32
	s_addc_u32 s5, s23, s25
	v_writelane_b32 v254, s4, 33
	s_ashr_i32 s41, s40, 31
	s_ashr_i32 s23, s22, 31
	v_writelane_b32 v254, s5, 34
	s_lshl_b64 s[4:5], s[40:41], 2
	v_writelane_b32 v254, s4, 35
	s_mul_i32 s2, s10, 0x60
	v_mov_b64_e32 v[238:239], 0x47f
	v_writelane_b32 v254, s5, 36
	s_lshl_b64 s[4:5], s[22:23], 2
	v_writelane_b32 v254, s4, 37
	v_mov_b32_e32 v234, 0x30000
	s_movk_i32 s59, 0x300
	v_writelane_b32 v254, s5, 38
	s_lshl_b64 s[4:5], s[40:41], 12
	v_writelane_b32 v254, s4, 39
	s_mov_b64 s[24:25], 0x80
	s_mov_b32 s96, 0x3e38aa3b
	v_writelane_b32 v254, s5, 40
	s_lshl_b64 s[4:5], s[22:23], 12
	v_writelane_b32 v254, s4, 41
	s_mov_b64 s[84:85], 0x2000
	s_mov_b32 s62, s89
	v_writelane_b32 v254, s5, 42
	s_mov_b32 s4, s40
	v_writelane_b32 v254, s4, 43
	s_nop 1
	v_writelane_b32 v254, s5, 44
	s_lshl_b64 s[4:5], s[40:41], 11
	v_writelane_b32 v254, s4, 45
	s_nop 1
	v_writelane_b32 v254, s5, 46
	s_mov_b32 s4, s22
	v_writelane_b32 v254, s4, 47
	s_nop 1
	v_writelane_b32 v254, s5, 48
	s_lshl_b64 s[4:5], s[22:23], 11
	v_writelane_b32 v254, s4, 49
	s_nop 1
	v_writelane_b32 v254, s5, 50
	s_add_u32 s4, s26, 0x2000000
	s_addc_u32 s5, s27, 0
	v_writelane_b32 v254, s4, 51
	s_lshl_b32 s2, s2, 1
	s_ashr_i32 s35, s34, 31
	v_writelane_b32 v254, s5, 52
	v_writelane_b32 v254, s2, 53
	v_writelane_b32 v254, s20, 54
	s_mov_b32 s2, s21
	s_lshl_b64 s[6:7], s[34:35], 6
	v_writelane_b32 v254, s21, 55
	v_writelane_b32 v254, s2, 56
	s_add_i32 s2, 0, 0x20400
	v_writelane_b32 v254, s2, 57
	s_add_i32 s2, 0, 0x25800
	v_writelane_b32 v254, s2, 58
	s_add_i32 s2, 0, 0x25804
	v_writelane_b32 v254, s2, 59
	s_add_i32 s2, 0, 0x20140
	v_writelane_b32 v254, s2, 60
	s_add_i32 s2, 0, 0x20150
	v_writelane_b32 v254, s2, 61
	s_add_i32 s2, 0, 0x20160
	v_writelane_b32 v254, s2, 62
	s_add_i32 s2, 0, 0x20170
	v_writelane_b32 v254, s2, 63
	s_add_i32 s2, 0, 0x20180
	v_writelane_b32 v255, s2, 0
	s_add_i32 s2, 0, 0x20190
	v_writelane_b32 v255, s2, 1
	s_add_i32 s2, 0, 0x201a0
	v_writelane_b32 v255, s2, 2
	s_add_i32 s2, 0, 0x201b0
	v_writelane_b32 v255, s2, 3
	s_add_i32 s2, 0, 0x20080
	v_writelane_b32 v255, s2, 4
	s_add_i32 s2, 0, 0x20004
	v_writelane_b32 v255, s2, 5
	v_cmp_eq_u32_e64 s[2:3], 0, v0
	s_lshl_b64 s[8:9], s[34:35], 5
	v_cmp_eq_u32_e64 s[4:5], 0, v2
	v_writelane_b32 v255, s2, 6
	s_nop 1
	v_writelane_b32 v255, s3, 7
	v_writelane_b32 v255, s78, 8
	v_writelane_b32 v255, s70, 9
	v_writelane_b32 v255, s71, 10
	v_writelane_b32 v255, s90, 11
	s_nop 1
	v_writelane_b32 v255, s91, 12
	v_writelane_b32 v255, s94, 13
	s_nop 1
	v_writelane_b32 v255, s95, 14
	v_writelane_b32 v255, s79, 15
	v_writelane_b32 v255, s61, 16
	v_writelane_b32 v255, s58, 17
	v_writelane_b32 v255, s55, 18
	v_writelane_b32 v255, s77, 19
	v_writelane_b32 v255, s80, 20
	s_nop 1
	v_writelane_b32 v255, s81, 21
	v_writelane_b32 v255, s82, 22
	s_nop 1
	v_writelane_b32 v255, s83, 23
	v_writelane_b32 v255, s97, 24
	v_writelane_b32 v255, s65, 25
	v_writelane_b32 v255, s34, 26
	s_nop 1
	v_writelane_b32 v255, s35, 27
	v_writelane_b32 v255, s6, 28
	s_nop 1
	v_writelane_b32 v255, s7, 29
	v_writelane_b32 v255, s8, 30
	s_nop 1
	v_writelane_b32 v255, s9, 31
	s_branch .LBB0_286

; __device__ __forceinline__ void phase_prep_moe(Frame& F, int l, int part) {
;     ...
;     const int k0 = part ? 1 : 0, k1 = part ? mult : 1;
;     for (int rnd = 0; rnd * slots < NEXP * I_E; ++rnd)
;       for (int k = k0; k < k1; ++k) {
;         const int it = rnd * slots + base + k; if (it >= NEXP * I_E) break;
;         const int e = it / I_E; int r = it % I_E;
;         if (r < I_G1) { const int kb = r >> 3, n0 = (r & 7) * 64; const int pn = n0 >> 8, c = n0 & 255;
.LBB0_289:
	s_min_u32 s8, s70, 1
	s_mov_b64 s[10:11], 0
	s_and_b64 vcc, exec, s[80:81]
	s_cbranch_vccnz .LBB0_597
.LBB0_290:
	s_xor_b64 s[80:81], s[10:11], -1
	s_add_u32 s2, s74, 0x3e00000
	v_lshlrev_b32_e32 v0, 2, v67
	s_addc_u32 s3, s75, 0
	v_lshrrev_b32_e32 v69, 4, v67
	v_and_b32_e32 v66, 60, v0
	s_add_u32 s6, s74, 0x5e00000
	v_lshlrev_b32_e32 v0, 2, v66
	v_mul_u32_u24_e32 v2, 0x104, v69
	s_addc_u32 s7, s75, 0
	v_add3_u32 v106, s78, v0, v2
	v_lshlrev_b32_e32 v2, 3, v67
	s_and_b64 s[12:13], s[10:11], exec
	v_lshrrev_b32_e32 v0, 3, v67
	v_and_b32_e32 v68, 56, v2
	s_cselect_b32 s9, 1, s70
	s_min_u32 s9, s9, s70
	v_mul_u32_u24_e32 v2, 0x104, v68
	v_lshlrev_b32_e32 v3, 2, v0
	s_cmp_lg_u32 s9, s8
	v_add3_u32 v107, s78, v2, v3
	v_or_b32_e32 v2, 8, v0
	v_or_b32_e32 v3, 16, v0
	v_or_b32_e32 v4, 24, v0
	v_or_b32_e32 v5, 32, v0
	v_or_b32_e32 v6, 40, v0
	v_or_b32_e32 v7, 48, v0
	v_or_b32_e32 v8, 56, v0
	s_cselect_b64 s[12:13], -1, 0
	v_lshlrev_b32_e32 v70, 9, v0
	v_mov_b32_e32 v71, v1
	v_lshlrev_b32_e32 v72, 9, v2
	v_mov_b32_e32 v73, v1
	v_lshlrev_b32_e32 v74, 9, v3
	v_mov_b32_e32 v75, v1
	v_lshlrev_b32_e32 v76, 9, v4
	v_mov_b32_e32 v77, v1
	v_lshlrev_b32_e32 v78, 9, v5
	v_mov_b32_e32 v79, v1
	v_lshlrev_b32_e32 v80, 9, v6
	v_mov_b32_e32 v81, v1
	v_lshlrev_b32_e32 v82, 9, v7
	v_mov_b32_e32 v83, v1
	v_lshlrev_b32_e32 v84, 9, v8
	v_mov_b32_e32 v85, v1
	v_lshlrev_b32_e32 v86, 11, v0
	v_mov_b32_e32 v87, v1
	v_lshlrev_b32_e32 v88, 11, v2
	v_mov_b32_e32 v89, v1
	v_lshlrev_b32_e32 v90, 11, v3
	v_mov_b32_e32 v91, v1
	v_lshlrev_b32_e32 v92, 11, v4
	v_mov_b32_e32 v93, v1
	v_lshlrev_b32_e32 v94, 11, v5
	v_mov_b32_e32 v95, v1
	v_lshlrev_b32_e32 v96, 11, v6
	v_mov_b32_e32 v97, v1
	v_lshlrev_b32_e32 v98, 11, v7
	v_mov_b32_e32 v99, v1
	v_lshlrev_b32_e32 v100, 11, v8
	v_mov_b32_e32 v101, v1
	s_sub_i32 s20, s9, s8
	s_add_i32 s21, s71, s8
	s_mov_b32 s8, 0
	v_add_u32_e32 v108, 0x410, v106
	v_add_u32_e32 v109, 0x418, v106
	v_add_u32_e32 v110, 0x820, v106
	s_mov_b32 s26, 0
	s_branch .LBB0_292
